# s36 + P0 mod hand-off: the 192 GEMV workgroups publish MOD with write-through (sc0 sc1) stores instead of a whole-L2 write-back (buffer_wbl2) each
# speedup vs baseline: 1.0180x; 1.0070x over previous
; __global__ void __launch_bounds__(NTHREADS, 2) fwd(Args args) {
;     ...
; #pragma unroll 16
;                 for (int kk = 0; kk < 64; ++kk) { const int k = kg * 64 + kk; const f32x4 w = *(const f32x4*)(w_ada + (size_t)k * (6 * D) + n0);
; #pragma unroll
;                     for (int r = 0; r < 5; ++r) { const float s = sc[r * D + k]; acc[r][0] += s * w.x; acc[r][1] += s * w.y; acc[r][2] += s * w.z; acc[r][3] += s * w.w; } }
.LBB0_19:
	v_lshl_add_u64 v[54:55], v[52:53], 0, s[4:5]
	ds_read_b128 v[20:23], v51
	ds_read_b128 v[16:19], v51 offset:16
	ds_read_b128 v[56:59], v51 offset:8192
	ds_read_b128 v[32:35], v51 offset:8208
	ds_read_b128 v[60:63], v51 offset:16384
	ds_read_b128 v[36:39], v51 offset:16400
	ds_read_b128 v[64:67], v51 offset:24576
	ds_read_b128 v[8:11], v51 offset:24592
	global_load_dwordx4 v[76:79], v[54:55], off
	s_mov_b32 s6, 0xc000
	v_add_co_u32_e64 v6, s[6:7], s6, v54
	s_add_u32 s4, s4, 0xc0000
	s_nop 0
	v_addc_co_u32_e64 v7, s[6:7], 0, v55, s[6:7]
	global_load_dwordx4 v[80:83], v[6:7], off
	s_mov_b32 s6, 0x18000
	s_addc_u32 s5, s5, 0
	s_cmp_lg_u32 s4, 0x300000
	s_waitcnt vmcnt(1) lgkmcnt(7)
	v_pk_fma_f32 v[6:7], v[76:77], v[20:21], v[12:13] op_sel_hi:[1,0,1]
	v_pk_fma_f32 v[30:31], v[78:79], v[20:21], v[14:15] op_sel_hi:[1,0,1]
	s_waitcnt lgkmcnt(1)
	v_pk_fma_f32 v[68:69], v[76:77], v[64:65], v[26:27] op_sel_hi:[1,0,1]
	ds_read_b128 v[24:27], v51 offset:32768
	ds_read_b128 v[12:15], v51 offset:32784
	v_pk_fma_f32 v[44:45], v[76:77], v[56:57], v[44:45] op_sel_hi:[1,0,1]
	v_pk_fma_f32 v[46:47], v[78:79], v[56:57], v[46:47] op_sel_hi:[1,0,1]
	v_pk_fma_f32 v[40:41], v[76:77], v[60:61], v[40:41] op_sel_hi:[1,0,1]
	v_pk_fma_f32 v[42:43], v[78:79], v[60:61], v[42:43] op_sel_hi:[1,0,1]
	v_pk_fma_f32 v[28:29], v[78:79], v[64:65], v[28:29] op_sel_hi:[1,0,1]
	s_waitcnt lgkmcnt(1)
	v_pk_fma_f32 v[2:3], v[76:77], v[24:25], v[2:3] op_sel_hi:[1,0,1]
	s_waitcnt vmcnt(0)
	v_pk_fma_f32 v[6:7], v[80:81], v[20:21], v[6:7] op_sel:[0,1,0]
	v_pk_fma_f32 v[20:21], v[82:83], v[20:21], v[30:31] op_sel:[0,1,0]
	v_pk_fma_f32 v[30:31], v[80:81], v[56:57], v[44:45] op_sel:[0,1,0]
	v_pk_fma_f32 v[44:45], v[82:83], v[56:57], v[46:47] op_sel:[0,1,0]
	v_pk_fma_f32 v[46:47], v[80:81], v[60:61], v[40:41] op_sel:[0,1,0]
	v_pk_fma_f32 v[56:57], v[82:83], v[60:61], v[42:43] op_sel:[0,1,0]
	v_pk_fma_f32 v[60:61], v[80:81], v[64:65], v[68:69] op_sel:[0,1,0]
	v_pk_fma_f32 v[28:29], v[82:83], v[64:65], v[28:29] op_sel:[0,1,0]
	v_pk_fma_f32 v[64:65], v[80:81], v[24:25], v[2:3] op_sel:[0,1,0]
	v_add_co_u32_e64 v2, s[6:7], s6, v54
	v_pk_fma_f32 v[4:5], v[78:79], v[24:25], v[4:5] op_sel_hi:[1,0,1]
	s_nop 0
	v_addc_co_u32_e64 v3, s[6:7], 0, v55, s[6:7]
	s_mov_b32 s6, 0x24000
	s_nop 0
	v_add_co_u32_e64 v40, s[6:7], s6, v54
	v_pk_fma_f32 v[24:25], v[82:83], v[24:25], v[4:5] op_sel:[0,1,0]
	s_nop 0
	v_addc_co_u32_e64 v41, s[6:7], 0, v55, s[6:7]
	global_load_dwordx4 v[2:5], v[2:3], off
	s_nop 0
	global_load_dwordx4 v[40:43], v[40:41], off
	s_mov_b32 s6, 0x30000
	v_mov_b32_e32 v68, v23
	v_mov_b32_e32 v70, v27
	s_waitcnt vmcnt(1)
	v_pk_fma_f32 v[30:31], v[2:3], v[58:59], v[30:31] op_sel_hi:[1,0,1]
	v_pk_fma_f32 v[44:45], v[4:5], v[58:59], v[44:45] op_sel_hi:[1,0,1]
	v_mov_b32_e32 v58, v59
	s_waitcnt vmcnt(0)
	v_pk_fma_f32 v[30:31], v[40:41], v[58:59], v[30:31] op_sel_hi:[1,0,1]
	v_pk_fma_f32 v[58:59], v[42:43], v[58:59], v[44:45] op_sel_hi:[1,0,1]
	v_add_co_u32_e64 v44, s[6:7], s6, v54
	v_pk_fma_f32 v[6:7], v[2:3], v[22:23], v[6:7] op_sel_hi:[1,0,1]
	s_nop 0
	v_addc_co_u32_e64 v45, s[6:7], 0, v55, s[6:7]
	v_pk_fma_f32 v[20:21], v[4:5], v[22:23], v[20:21] op_sel_hi:[1,0,1]
	v_pk_fma_f32 v[46:47], v[2:3], v[62:63], v[46:47] op_sel_hi:[1,0,1]
	v_pk_fma_f32 v[56:57], v[4:5], v[62:63], v[56:57] op_sel_hi:[1,0,1]
	v_mov_b32_e32 v62, v63
	s_mov_b32 s6, 0x3c000
	v_pk_fma_f32 v[6:7], v[40:41], v[68:69], v[6:7] op_sel_hi:[1,0,1]
	v_pk_fma_f32 v[20:21], v[42:43], v[68:69], v[20:21] op_sel_hi:[1,0,1]
	v_pk_fma_f32 v[68:69], v[40:41], v[62:63], v[46:47] op_sel_hi:[1,0,1]
	v_add_co_u32_e64 v46, s[6:7], s6, v54
	v_pk_fma_f32 v[60:61], v[2:3], v[66:67], v[60:61] op_sel_hi:[1,0,1]
	v_pk_fma_f32 v[76:77], v[4:5], v[66:67], v[28:29] op_sel_hi:[1,0,1]
	v_pk_fma_f32 v[64:65], v[2:3], v[26:27], v[64:65] op_sel_hi:[1,0,1]
	v_pk_fma_f32 v[78:79], v[4:5], v[26:27], v[24:25] op_sel_hi:[1,0,1]
	v_mov_b32_e32 v66, v67
	v_addc_co_u32_e64 v47, s[6:7], 0, v55, s[6:7]
	ds_read_b128 v[22:25], v51 offset:32
	ds_read_b128 v[2:5], v51 offset:48
	ds_read_b128 v[26:29], v51 offset:8224
	v_pk_fma_f32 v[56:57], v[42:43], v[62:63], v[56:57] op_sel_hi:[1,0,1]
	v_pk_fma_f32 v[60:61], v[40:41], v[66:67], v[60:61] op_sel_hi:[1,0,1]
	v_pk_fma_f32 v[62:63], v[42:43], v[66:67], v[76:77] op_sel_hi:[1,0,1]
	v_pk_fma_f32 v[64:65], v[40:41], v[70:71], v[64:65] op_sel_hi:[1,0,1]
	v_pk_fma_f32 v[66:67], v[42:43], v[70:71], v[78:79] op_sel_hi:[1,0,1]
	global_load_dwordx4 v[40:43], v[44:45], off
	s_nop 0
	global_load_dwordx4 v[44:47], v[46:47], off
	s_mov_b32 s6, 0x48000
	v_add_co_u32_e64 v76, s[6:7], s6, v54
	v_mov_b32_e32 v70, v35
	s_nop 0
	v_addc_co_u32_e64 v77, s[6:7], 0, v55, s[6:7]
	s_mov_b32 s6, 0x54000
	s_waitcnt vmcnt(1)
	v_pk_fma_f32 v[6:7], v[40:41], v[16:17], v[6:7] op_sel_hi:[1,0,1]
	v_pk_fma_f32 v[30:31], v[40:41], v[32:33], v[30:31] op_sel_hi:[1,0,1]
	v_pk_fma_f32 v[68:69], v[40:41], v[36:37], v[68:69] op_sel_hi:[1,0,1]
	v_pk_fma_f32 v[78:79], v[40:41], v[8:9], v[60:61] op_sel_hi:[1,0,1]
	s_waitcnt lgkmcnt(3)
	v_pk_fma_f32 v[40:41], v[40:41], v[12:13], v[64:65] op_sel_hi:[1,0,1]
	v_add_co_u32_e64 v64, s[6:7], s6, v54
	v_pk_fma_f32 v[20:21], v[42:43], v[16:17], v[20:21] op_sel_hi:[1,0,1]
	v_pk_fma_f32 v[58:59], v[42:43], v[32:33], v[58:59] op_sel_hi:[1,0,1]
	v_pk_fma_f32 v[56:57], v[42:43], v[36:37], v[56:57] op_sel_hi:[1,0,1]
	v_pk_fma_f32 v[80:81], v[42:43], v[8:9], v[62:63] op_sel_hi:[1,0,1]
	v_pk_fma_f32 v[42:43], v[42:43], v[12:13], v[66:67] op_sel_hi:[1,0,1]
	v_addc_co_u32_e64 v65, s[6:7], 0, v55, s[6:7]
	global_load_dwordx4 v[60:63], v[76:77], off
	s_waitcnt vmcnt(1)
; __global__ void __launch_bounds__(NTHREADS, 2) fwd(Args args) {
;     ...
; #pragma unroll 16
;                 for (int kk = 0; kk < 64; ++kk) { const int k = kg * 64 + kk; const f32x4 w = *(const f32x4*)(w_ada + (size_t)k * (6 * D) + n0);
; #pragma unroll
;                     for (int r = 0; r < 5; ++r) { const float s = sc[r * D + k]; acc[r][0] += s * w.x; acc[r][1] += s * w.y; acc[r][2] += s * w.z; acc[r][3] += s * w.w; } }
	v_pk_fma_f32 v[76:77], v[44:45], v[12:13], v[40:41] op_sel:[0,1,0]
	v_pk_fma_f32 v[12:13], v[46:47], v[12:13], v[42:43] op_sel:[0,1,0]
	global_load_dwordx4 v[40:43], v[64:65], off
	v_pk_fma_f32 v[58:59], v[46:47], v[32:33], v[58:59] op_sel:[0,1,0]
	v_pk_fma_f32 v[66:67], v[44:45], v[36:37], v[68:69] op_sel:[0,1,0]
	v_pk_fma_f32 v[36:37], v[46:47], v[36:37], v[56:57] op_sel:[0,1,0]
	v_pk_fma_f32 v[6:7], v[44:45], v[16:17], v[6:7] op_sel:[0,1,0]
	v_pk_fma_f32 v[16:17], v[46:47], v[16:17], v[20:21] op_sel:[0,1,0]
	v_pk_fma_f32 v[68:69], v[44:45], v[8:9], v[78:79] op_sel:[0,1,0]
	v_pk_fma_f32 v[8:9], v[46:47], v[8:9], v[80:81] op_sel:[0,1,0]
	v_mov_b32_e32 v46, v39
	s_mov_b32 s6, 0x60000
	v_pk_fma_f32 v[20:21], v[44:45], v[32:33], v[30:31] op_sel:[0,1,0]
	v_mov_b32_e32 v64, v19
	ds_read_b128 v[30:33], v51 offset:16416
	s_waitcnt vmcnt(1)
	v_pk_fma_f32 v[82:83], v[62:63], v[34:35], v[58:59] op_sel_hi:[1,0,1]
	v_pk_fma_f32 v[56:57], v[60:61], v[38:39], v[66:67] op_sel_hi:[1,0,1]
	v_pk_fma_f32 v[58:59], v[62:63], v[38:39], v[36:37] op_sel_hi:[1,0,1]
	s_waitcnt vmcnt(0)
	v_pk_fma_f32 v[56:57], v[40:41], v[46:47], v[56:57] op_sel_hi:[1,0,1]
	v_pk_fma_f32 v[46:47], v[42:43], v[46:47], v[58:59] op_sel_hi:[1,0,1]
	v_add_co_u32_e64 v58, s[6:7], s6, v54
	v_pk_fma_f32 v[78:79], v[60:61], v[18:19], v[6:7] op_sel_hi:[1,0,1]
	v_pk_fma_f32 v[16:17], v[62:63], v[18:19], v[16:17] op_sel_hi:[1,0,1]
	v_pk_fma_f32 v[80:81], v[60:61], v[34:35], v[20:21] op_sel_hi:[1,0,1]
	v_pk_fma_f32 v[38:39], v[60:61], v[10:11], v[68:69] op_sel_hi:[1,0,1]
	v_pk_fma_f32 v[44:45], v[62:63], v[10:11], v[8:9] op_sel_hi:[1,0,1]
	v_pk_fma_f32 v[18:19], v[60:61], v[14:15], v[76:77] op_sel_hi:[1,0,1]
	v_mov_b32_e32 v60, v11
	v_addc_co_u32_e64 v59, s[6:7], 0, v55, s[6:7]
	v_pk_fma_f32 v[66:67], v[40:41], v[64:65], v[78:79] op_sel_hi:[1,0,1]
	v_pk_fma_f32 v[78:79], v[40:41], v[60:61], v[38:39] op_sel_hi:[1,0,1]
	v_pk_fma_f32 v[60:61], v[42:43], v[60:61], v[44:45] op_sel_hi:[1,0,1]
	v_add_co_u32_e64 v44, s[6:7], s3, v54
	v_pk_fma_f32 v[20:21], v[62:63], v[14:15], v[12:13] op_sel_hi:[1,0,1]
	v_mov_b32_e32 v62, v15
	v_addc_co_u32_e64 v45, s[6:7], 0, v55, s[6:7]
	ds_read_b128 v[34:37], v51 offset:24608
	ds_read_b128 v[10:13], v51 offset:16432
	ds_read_b128 v[6:9], v51 offset:8240
	v_pk_fma_f32 v[64:65], v[42:43], v[64:65], v[16:17] op_sel_hi:[1,0,1]
	v_pk_fma_f32 v[68:69], v[40:41], v[70:71], v[80:81] op_sel_hi:[1,0,1]
	v_pk_fma_f32 v[76:77], v[42:43], v[70:71], v[82:83] op_sel_hi:[1,0,1]
	ds_read_b128 v[14:17], v51 offset:24624
	v_pk_fma_f32 v[80:81], v[40:41], v[62:63], v[18:19] op_sel_hi:[1,0,1]
	v_pk_fma_f32 v[62:63], v[42:43], v[62:63], v[20:21] op_sel_hi:[1,0,1]
	global_load_dwordx4 v[38:41], v[58:59], off
	s_nop 0
	global_load_dwordx4 v[42:45], v[44:45], off
	s_waitcnt lgkmcnt(3)
	v_mov_b32_e32 v70, v37
	s_waitcnt vmcnt(1)
	v_pk_fma_f32 v[82:83], v[38:39], v[30:31], v[56:57] op_sel_hi:[1,0,1]
	ds_read_b128 v[56:59], v51 offset:32800
	ds_read_b128 v[18:21], v51 offset:32816
	v_pk_fma_f32 v[66:67], v[38:39], v[22:23], v[66:67] op_sel_hi:[1,0,1]
	v_pk_fma_f32 v[68:69], v[38:39], v[26:27], v[68:69] op_sel_hi:[1,0,1]
	v_pk_fma_f32 v[46:47], v[40:41], v[30:31], v[46:47] op_sel_hi:[1,0,1]
	v_pk_fma_f32 v[78:79], v[38:39], v[34:35], v[78:79] op_sel_hi:[1,0,1]
	v_pk_fma_f32 v[60:61], v[40:41], v[34:35], v[60:61] op_sel_hi:[1,0,1]
	s_waitcnt lgkmcnt(1)
	v_pk_fma_f32 v[38:39], v[38:39], v[56:57], v[80:81] op_sel_hi:[1,0,1]
	v_pk_fma_f32 v[64:65], v[40:41], v[22:23], v[64:65] op_sel_hi:[1,0,1]
	v_pk_fma_f32 v[76:77], v[40:41], v[26:27], v[76:77] op_sel_hi:[1,0,1]
	v_pk_fma_f32 v[40:41], v[40:41], v[56:57], v[62:63] op_sel_hi:[1,0,1]
	s_waitcnt vmcnt(0)
	v_pk_fma_f32 v[62:63], v[42:43], v[22:23], v[66:67] op_sel:[0,1,0]
	v_pk_fma_f32 v[66:67], v[42:43], v[30:31], v[82:83] op_sel:[0,1,0]
	v_pk_fma_f32 v[30:31], v[44:45], v[30:31], v[46:47] op_sel:[0,1,0]
	v_pk_fma_f32 v[46:47], v[42:43], v[34:35], v[78:79] op_sel:[0,1,0]
	v_pk_fma_f32 v[34:35], v[44:45], v[34:35], v[60:61] op_sel:[0,1,0]
	v_pk_fma_f32 v[60:61], v[42:43], v[56:57], v[38:39] op_sel:[0,1,0]
	v_add_co_u32_e64 v38, s[6:7], s8, v54
	v_pk_fma_f32 v[56:57], v[44:45], v[56:57], v[40:41] op_sel:[0,1,0]
	s_nop 0
	v_addc_co_u32_e64 v39, s[6:7], 0, v55, s[6:7]
	v_add_co_u32_e64 v40, s[6:7], s9, v54
	v_pk_fma_f32 v[22:23], v[44:45], v[22:23], v[64:65] op_sel:[0,1,0]
	s_nop 0
	v_addc_co_u32_e64 v41, s[6:7], 0, v55, s[6:7]
	v_pk_fma_f32 v[64:65], v[42:43], v[26:27], v[68:69] op_sel:[0,1,0]
	v_pk_fma_f32 v[26:27], v[44:45], v[26:27], v[76:77] op_sel:[0,1,0]
	global_load_dwordx4 v[42:45], v[38:39], off
	s_nop 0
	global_load_dwordx4 v[38:41], v[40:41], off
	v_add_u32_e32 v51, 64, v51
	s_waitcnt vmcnt(1)
	v_pk_fma_f32 v[82:83], v[44:45], v[32:33], v[30:31] op_sel_hi:[1,0,1]
	v_add_co_u32_e64 v30, s[6:7], s10, v54
	v_pk_fma_f32 v[80:81], v[42:43], v[32:33], v[66:67] op_sel_hi:[1,0,1]
	s_nop 0
	v_addc_co_u32_e64 v31, s[6:7], 0, v55, s[6:7]
	v_pk_fma_f32 v[66:67], v[42:43], v[36:37], v[46:47] op_sel_hi:[1,0,1]
	v_add_co_u32_e64 v46, s[6:7], s11, v54
	v_pk_fma_f32 v[76:77], v[42:43], v[24:25], v[62:63] op_sel_hi:[1,0,1]
	s_nop 0
	v_addc_co_u32_e64 v47, s[6:7], 0, v55, s[6:7]
	v_pk_fma_f32 v[62:63], v[44:45], v[58:59], v[56:57] op_sel_hi:[1,0,1]
	v_add_co_u32_e64 v56, s[6:7], s12, v54
	v_pk_fma_f32 v[22:23], v[44:45], v[24:25], v[22:23] op_sel_hi:[1,0,1]
	s_nop 0
	v_addc_co_u32_e64 v57, s[6:7], 0, v55, s[6:7]
	v_add_co_u32_e64 v84, s[6:7], s13, v54
	v_pk_fma_f32 v[68:69], v[44:45], v[36:37], v[34:35] op_sel_hi:[1,0,1]
	s_nop 0
	v_addc_co_u32_e64 v85, s[6:7], 0, v55, s[6:7]
	v_mov_b32_e32 v24, v25
	global_load_dwordx4 v[34:37], v[30:31], off
	v_pk_fma_f32 v[78:79], v[42:43], v[28:29], v[64:65] op_sel_hi:[1,0,1]
	v_pk_fma_f32 v[26:27], v[44:45], v[28:29], v[26:27] op_sel_hi:[1,0,1]
	v_pk_fma_f32 v[60:61], v[42:43], v[58:59], v[60:61] op_sel_hi:[1,0,1]
	v_mov_b32_e32 v28, v29
	v_mov_b32_e32 v58, v33
	s_waitcnt vmcnt(1)
; #define LBAR() do { asm volatile("s_waitcnt lgkmcnt(0)" ::: "memory"); __builtin_amdgcn_s_barrier(); asm volatile("" ::: "memory"); } while (0)
; __global__ void __launch_bounds__(NTHREADS, 2) fwd(Args args) {
;     ...
;                 for (int kk = 0; kk < 64; ++kk) { const int k = kg * 64 + kk; const f32x4 w = *(const f32x4*)(w_ada + (size_t)k * (6 * D) + n0);
; #pragma unroll
;                     for (int r = 0; r < 5; ++r) { const float s = sc[r * D + k]; acc[r][0] += s * w.x; acc[r][1] += s * w.y; acc[r][2] += s * w.z; acc[r][3] += s * w.w; } }
; #pragma unroll
;                 for (int r = 0; r < 5; ++r)
; #pragma unroll
;                     for (int j = 0; j < 4; ++j) red[(kg * 5 + r) * 64 + cg * 4 + j] = acc[r][j];
;                 LBAR();
;                 if (tid < 320) { const int r = tid / 64, cidx = tid % 64; float s = 0.f;
;                     for (int g2 = 0; g2 < 32; ++g2) s += red[(g2 * 5 + r) * 64 + cidx];
;                     MOD[r * (6 * D) + u * 64 + cidx] = s + b_ada[u * 64 + cidx]; }
	v_pk_fma_f32 v[42:43], v[38:39], v[24:25], v[76:77] op_sel_hi:[1,0,1]
	v_pk_fma_f32 v[44:45], v[40:41], v[24:25], v[22:23] op_sel_hi:[1,0,1]
	global_load_dwordx4 v[22:25], v[84:85], off
	global_load_dwordx4 v[30:33], v[46:47], off
	v_pk_fma_f32 v[46:47], v[38:39], v[28:29], v[78:79] op_sel_hi:[1,0,1]
	v_pk_fma_f32 v[54:55], v[40:41], v[28:29], v[26:27] op_sel_hi:[1,0,1]
	global_load_dwordx4 v[26:29], v[56:57], off
	v_mov_b32_e32 v64, v59
	v_pk_fma_f32 v[56:57], v[38:39], v[58:59], v[80:81] op_sel_hi:[1,0,1]
	v_pk_fma_f32 v[58:59], v[40:41], v[58:59], v[82:83] op_sel_hi:[1,0,1]
	v_pk_fma_f32 v[76:77], v[38:39], v[70:71], v[66:67] op_sel_hi:[1,0,1]
	v_pk_fma_f32 v[68:69], v[40:41], v[70:71], v[68:69] op_sel_hi:[1,0,1]
	v_pk_fma_f32 v[78:79], v[38:39], v[64:65], v[60:61] op_sel_hi:[1,0,1]
	v_pk_fma_f32 v[80:81], v[40:41], v[64:65], v[62:63] op_sel_hi:[1,0,1]
	v_mov_b32_e32 v66, v5
	v_mov_b32_e32 v40, v9
	v_mov_b32_e32 v38, v13
	v_mov_b32_e32 v60, v17
	s_waitcnt vmcnt(3)
	v_pk_fma_f32 v[42:43], v[34:35], v[2:3], v[42:43] op_sel_hi:[1,0,1]
	v_pk_fma_f32 v[44:45], v[36:37], v[2:3], v[44:45] op_sel_hi:[1,0,1]
	v_pk_fma_f32 v[46:47], v[34:35], v[6:7], v[46:47] op_sel_hi:[1,0,1]
	v_pk_fma_f32 v[54:55], v[36:37], v[6:7], v[54:55] op_sel_hi:[1,0,1]
	v_pk_fma_f32 v[56:57], v[34:35], v[10:11], v[56:57] op_sel_hi:[1,0,1]
	v_pk_fma_f32 v[58:59], v[36:37], v[10:11], v[58:59] op_sel_hi:[1,0,1]
	v_pk_fma_f32 v[62:63], v[34:35], v[14:15], v[76:77] op_sel_hi:[1,0,1]
	v_pk_fma_f32 v[64:65], v[36:37], v[14:15], v[68:69] op_sel_hi:[1,0,1]
	s_waitcnt lgkmcnt(0)
	v_pk_fma_f32 v[34:35], v[34:35], v[18:19], v[78:79] op_sel_hi:[1,0,1]
	v_pk_fma_f32 v[36:37], v[36:37], v[18:19], v[80:81] op_sel_hi:[1,0,1]
	s_waitcnt vmcnt(1)
	v_pk_fma_f32 v[42:43], v[30:31], v[2:3], v[42:43] op_sel:[0,1,0]
	v_pk_fma_f32 v[2:3], v[32:33], v[2:3], v[44:45] op_sel:[0,1,0]
	v_pk_fma_f32 v[44:45], v[30:31], v[6:7], v[46:47] op_sel:[0,1,0]
	v_pk_fma_f32 v[6:7], v[32:33], v[6:7], v[54:55] op_sel:[0,1,0]
	v_pk_fma_f32 v[46:47], v[30:31], v[10:11], v[56:57] op_sel:[0,1,0]
	v_pk_fma_f32 v[10:11], v[32:33], v[10:11], v[58:59] op_sel:[0,1,0]
	v_pk_fma_f32 v[54:55], v[30:31], v[14:15], v[62:63] op_sel:[0,1,0]
	v_pk_fma_f32 v[14:15], v[32:33], v[14:15], v[64:65] op_sel:[0,1,0]
	v_pk_fma_f32 v[30:31], v[30:31], v[18:19], v[34:35] op_sel:[0,1,0]
	v_pk_fma_f32 v[18:19], v[32:33], v[18:19], v[36:37] op_sel:[0,1,0]
	v_mov_b32_e32 v68, v21
	s_waitcnt vmcnt(0)
	v_pk_fma_f32 v[32:33], v[26:27], v[4:5], v[42:43] op_sel_hi:[1,0,1]
	v_pk_fma_f32 v[2:3], v[28:29], v[4:5], v[2:3] op_sel_hi:[1,0,1]
	v_pk_fma_f32 v[4:5], v[26:27], v[8:9], v[44:45] op_sel_hi:[1,0,1]
	v_pk_fma_f32 v[6:7], v[28:29], v[8:9], v[6:7] op_sel_hi:[1,0,1]
	v_pk_fma_f32 v[8:9], v[26:27], v[12:13], v[46:47] op_sel_hi:[1,0,1]
	v_pk_fma_f32 v[10:11], v[28:29], v[12:13], v[10:11] op_sel_hi:[1,0,1]
	v_pk_fma_f32 v[34:35], v[26:27], v[16:17], v[54:55] op_sel_hi:[1,0,1]
	v_pk_fma_f32 v[16:17], v[28:29], v[16:17], v[14:15] op_sel_hi:[1,0,1]
	v_pk_fma_f32 v[30:31], v[26:27], v[20:21], v[30:31] op_sel_hi:[1,0,1]
	v_pk_fma_f32 v[18:19], v[28:29], v[20:21], v[18:19] op_sel_hi:[1,0,1]
	v_pk_fma_f32 v[12:13], v[22:23], v[66:67], v[32:33] op_sel_hi:[1,0,1]
	v_pk_fma_f32 v[14:15], v[24:25], v[66:67], v[2:3] op_sel_hi:[1,0,1]
	v_pk_fma_f32 v[44:45], v[22:23], v[40:41], v[4:5] op_sel_hi:[1,0,1]
	v_pk_fma_f32 v[46:47], v[24:25], v[40:41], v[6:7] op_sel_hi:[1,0,1]
	v_pk_fma_f32 v[40:41], v[22:23], v[38:39], v[8:9] op_sel_hi:[1,0,1]
	v_pk_fma_f32 v[42:43], v[24:25], v[38:39], v[10:11] op_sel_hi:[1,0,1]
	v_pk_fma_f32 v[26:27], v[22:23], v[60:61], v[34:35] op_sel_hi:[1,0,1]
	v_pk_fma_f32 v[28:29], v[24:25], v[60:61], v[16:17] op_sel_hi:[1,0,1]
	v_pk_fma_f32 v[2:3], v[22:23], v[68:69], v[30:31] op_sel_hi:[1,0,1]
	v_pk_fma_f32 v[4:5], v[24:25], v[68:69], v[18:19] op_sel_hi:[1,0,1]
	s_cbranch_scc1 .LBB0_19
	ds_write_b128 v74, v[12:15] offset:40960
	ds_write_b128 v74, v[44:47] offset:41216
	ds_write_b128 v74, v[40:43] offset:41472
	ds_write_b128 v74, v[26:29] offset:41728
	ds_write_b128 v74, v[2:5] offset:41984
	s_waitcnt lgkmcnt(0)
	s_barrier
	s_and_saveexec_b64 s[4:5], vcc
	s_cbranch_execz .LBB0_17
	s_lshl_b32 s6, s18, 6
	v_or_b32_e32 v2, s6, v220
	v_ashrrev_i32_e32 v3, 31, v2
	v_lshl_add_u64 v[2:3], v[2:3], 2, s[30:31]
	global_load_dword v36, v[2:3], off
	ds_read2st64_b32 v[2:3], v71 offset0:160 offset1:165
	ds_read2st64_b32 v[4:5], v71 offset0:170 offset1:175
	ds_read2st64_b32 v[6:7], v71 offset0:180 offset1:185
	ds_read2st64_b32 v[8:9], v71 offset0:190 offset1:195
	ds_read2st64_b32 v[10:11], v71 offset0:200 offset1:205
	ds_read2st64_b32 v[12:13], v71 offset0:210 offset1:215
	ds_read2st64_b32 v[14:15], v71 offset0:220 offset1:225
	ds_read2st64_b32 v[16:17], v71 offset0:230 offset1:235
	ds_read2st64_b32 v[18:19], v71 offset0:240 offset1:245
	ds_read2st64_b32 v[20:21], v71 offset0:250 offset1:255
	ds_read2st64_b32 v[22:23], v72 offset0:100 offset1:105
	ds_read2st64_b32 v[24:25], v72 offset0:110 offset1:115
	ds_read2st64_b32 v[26:27], v72 offset0:120 offset1:125
	ds_read2st64_b32 v[28:29], v72 offset0:130 offset1:135
	ds_read2st64_b32 v[30:31], v72 offset0:140 offset1:145
	ds_read2st64_b32 v[32:33], v72 offset0:150 offset1:155
	s_waitcnt lgkmcnt(14)
	v_add_f32_e32 v2, 0, v2
	v_add_f32_e32 v2, v2, v3
	v_add_f32_e32 v2, v2, v4
	v_add_f32_e32 v2, v2, v5
	s_waitcnt lgkmcnt(13)
	v_add_f32_e32 v2, v2, v6
	v_add_f32_e32 v2, v2, v7
	s_waitcnt lgkmcnt(12)
	v_add_f32_e32 v2, v2, v8
	v_add_f32_e32 v2, v2, v9
	s_waitcnt lgkmcnt(11)
	v_add_f32_e32 v2, v2, v10
	v_add_f32_e32 v2, v2, v11
	s_waitcnt lgkmcnt(10)
	v_add_f32_e32 v2, v2, v12
	v_add_f32_e32 v2, v2, v13
	s_waitcnt lgkmcnt(9)
	v_add_f32_e32 v2, v2, v14
	v_add_f32_e32 v2, v2, v15
	s_waitcnt lgkmcnt(8)
	v_add_f32_e32 v2, v2, v16
	v_add_f32_e32 v2, v2, v17
	s_waitcnt lgkmcnt(7)
	v_add_f32_e32 v2, v2, v18
	v_add_f32_e32 v2, v2, v19
	s_waitcnt lgkmcnt(6)
	v_add_f32_e32 v2, v2, v20
	v_add_f32_e32 v2, v2, v21
	s_waitcnt lgkmcnt(5)
	v_add_f32_e32 v2, v2, v22
	v_add_f32_e32 v2, v2, v23
	s_waitcnt lgkmcnt(4)
	v_add_f32_e32 v2, v2, v24
	v_add_f32_e32 v2, v2, v25
	s_waitcnt lgkmcnt(3)
	v_add_f32_e32 v2, v2, v26
	v_add_f32_e32 v2, v2, v27
	s_waitcnt lgkmcnt(2)
	v_add_f32_e32 v2, v2, v28
	v_add_f32_e32 v2, v2, v29
	s_waitcnt lgkmcnt(1)
	v_add_f32_e32 v2, v2, v30
	v_add_f32_e32 v2, v2, v31
	v_add_u32_e32 v34, s6, v1
	s_waitcnt lgkmcnt(0)
	v_add_f32_e32 v2, v2, v32
	v_ashrrev_i32_e32 v35, 31, v34
	v_add_f32_e32 v2, v2, v33
	s_waitcnt vmcnt(0)
	v_add_f32_e32 v4, v2, v36
	v_lshl_add_u64 v[2:3], v[34:35], 2, s[96:97]
	global_store_dword v[2:3], v4, off sc0 sc1
	s_branch .LBB0_17
; #define LBAR() do { asm volatile("s_waitcnt lgkmcnt(0)" ::: "memory"); __builtin_amdgcn_s_barrier(); asm volatile("" ::: "memory"); } while (0)
; __global__ void __launch_bounds__(NTHREADS, 2) fwd(Args args) {
;     ...
;                 LBAR();
;             }
;             LBAR();
;             asm volatile("s_waitcnt vmcnt(0)" ::: "memory"); __syncthreads();
;             if (tid == 0 && bid < 192) { __builtin_amdgcn_fence(__ATOMIC_RELEASE, "agent"); asm volatile("s_waitcnt vmcnt(0)" ::: "memory"); __hip_atomic_fetch_add(ctl + CW_MODCNT, 1u, RLX_AGENT); }
.LBB0_22:
	s_waitcnt lgkmcnt(0)
	s_barrier
	s_waitcnt vmcnt(0)
	v_readlane_b32 s2, v246, 17
	v_readlane_b32 s3, v246, 18
	s_and_b64 s[2:3], s[2:3], s[0:1]
	s_waitcnt lgkmcnt(0)
	s_barrier
	s_and_saveexec_b64 s[0:1], s[2:3]
	s_cbranch_execz .LBB0_25
	s_mov_b64 s[4:5], exec
	v_mbcnt_lo_u32_b32 v1, s4, 0
	s_waitcnt vmcnt(0)
	s_waitcnt vmcnt(0)
	v_mbcnt_hi_u32_b32 v1, s5, v1
	v_cmp_eq_u32_e32 vcc, 0, v1
	s_and_b64 s[2:3], exec, vcc
	s_mov_b64 exec, s[2:3]
	s_cbranch_execz .LBB0_25
	s_bcnt1_i32_b64 s2, s[4:5]
	v_mov_b32_e32 v1, 0x3000
	v_mov_b32_e32 v2, s2
	global_atomic_add v1, v2, s[88:89] offset:2048
